# speedup vs baseline: 1.0102x; 1.0066x over previous
.Lp_next:
	s_setprio 2
	s_mov_b64 exec, 1
	ds_add_rtn_u32 v10, v59, v60
	s_mov_b64 exec, -1
	s_waitcnt lgkmcnt(0)
	v_readfirstlane_b32 s34, v10
	s_cmp_lt_u32 s34, s62
	s_cselect_b32 s45, s64, s65
	s_cselect_b32 s46, 0, s62
	s_cselect_b32 s48, s62, s63
	s_sub_u32 s47, s34, s46
	s_cmp_ge_u32 s47, s48
	s_cbranch_scc1 .Lp_done
	s_lshl_b32 s47, s47, 3
	s_add_u32 s45, s45, s47
	v_mov_b32_e32 v11, s45
	ds_read2_b32 v[12:13], v11 offset1:1
	s_waitcnt lgkmcnt(0)
	v_readfirstlane_b32 s35, v12
	v_readfirstlane_b32 s36, v13
	s_nop 1
	v_mov_b32_e32 v10, s35
	v_mov_b32_e32 v11, s36
	v_cndmask_b32_e64 v12, v10, v11, s[54:55]
	v_cndmask_b32_e64 v13, v10, v11, s[56:57]
	v_lshl_add_u32 v12, v12, 3, v61
	v_lshl_add_u32 v14, v13, 4, v62
	ds_read_b64 v[2:3], v12
	ds_read_b128 v[4:7], v14
	v_mad_u32_u24 v9, v13, s49, v58
	v_mov_b32_e32 v8, v56
	s_waitcnt lgkmcnt(0)
	v_add_u32_e32 v2, v2, v55
	v_and_b32_e32 v3, v3, v63
	s_nop 0
	v_readlane_b32 s41, v3, 0
	v_readlane_b32 s42, v3, 4
	s_max_u32 s43, s41, s42
	s_cmp_eq_u32 s43, 0
	s_cbranch_scc1 .Lp_zero
	ds_read_b64 v[36:37], v2
	v_cmp_gt_u32_e32 vcc, v3, v8
	v_add_u32_e32 v2, 64, v2
	v_add_u32_e32 v8, 16, v8
	v_mov_b32_e32 v33, 0x3c00
	s_waitcnt lgkmcnt(0)
	v_perm_b32 v32, v37, v36, v57
	v_cndmask_b32_e32 v33, 0, v33, vcc
	s_nop 0
	v_cndmask_b32_e32 v32, 0, v32, vcc
	s_nop 1
	v_mfma_f32_32x32x16_f16 v[96:111], v[32:35], v[64:67], 0
	v_mfma_f32_32x32x16_f16 v[112:127], v[32:35], v[68:71], 0
	s_setprio 0
	s_nop 10
	s_mov_b32 s45, s43
	s_min_u32 s46, s45, 16
	s_cmp_eq_u32 s46, 16
	s_cbranch_scc1 .Lf16
	s_cmp_eq_u32 s46, 15
	s_cbranch_scc1 .Lf15
	s_cmp_eq_u32 s46, 14
	s_cbranch_scc1 .Lf14
	s_cmp_eq_u32 s46, 13
	s_cbranch_scc1 .Lf13
	s_cmp_eq_u32 s46, 12
	s_cbranch_scc1 .Lf12
	s_cmp_eq_u32 s46, 11
	s_cbranch_scc1 .Lf11
	s_cmp_eq_u32 s46, 10
	s_cbranch_scc1 .Lf10
	s_cmp_eq_u32 s46, 9
	s_cbranch_scc1 .Lf9
	s_cmp_eq_u32 s46, 8
	s_cbranch_scc1 .Lf8
	s_cmp_eq_u32 s46, 7
	s_cbranch_scc1 .Lf7
	s_cmp_eq_u32 s46, 6
	s_cbranch_scc1 .Lf6
	s_cmp_eq_u32 s46, 5
	s_cbranch_scc1 .Lf5
	s_cmp_eq_u32 s46, 4
	s_cbranch_scc1 .Lf4
	s_cmp_eq_u32 s46, 3
	s_cbranch_scc1 .Lf3
	s_cmp_eq_u32 s46, 2
	s_cbranch_scc1 .Lf2

.Lsub:
	s_setprio 2
	ds_read_b64 v[36:37], v2
	v_cmp_gt_u32_e32 vcc, v3, v8
	v_add_u32_e32 v2, 64, v2
	v_add_u32_e32 v8, 16, v8
	v_mov_b32_e32 v33, 0x3c00
	s_waitcnt lgkmcnt(0)
	v_perm_b32 v32, v37, v36, v57
	v_cndmask_b32_e32 v33, 0, v33, vcc
	s_nop 0
	v_cndmask_b32_e32 v32, 0, v32, vcc
	s_nop 1
	v_mfma_f32_32x32x16_f16 v[96:111], v[32:35], v[64:67], 0
	v_mfma_f32_32x32x16_f16 v[112:127], v[32:35], v[68:71], 0
	s_setprio 0
	s_nop 10
	s_sub_u32 s45, s43, s44
	s_min_u32 s46, s45, 16
	s_cmp_eq_u32 s46, 2
	s_cbranch_scc1 .Ln2
	s_cmp_eq_u32 s46, 3
	s_cbranch_scc1 .Ln3
	s_cmp_eq_u32 s46, 4
	s_cbranch_scc1 .Ln4
	s_cmp_eq_u32 s46, 5
	s_cbranch_scc1 .Ln5
	s_cmp_eq_u32 s46, 6
	s_cbranch_scc1 .Ln6
	s_cmp_eq_u32 s46, 7
	s_cbranch_scc1 .Ln7
	s_cmp_eq_u32 s46, 8
	s_cbranch_scc1 .Ln8
	s_cmp_eq_u32 s46, 9
	s_cbranch_scc1 .Ln9
	s_cmp_eq_u32 s46, 10
	s_cbranch_scc1 .Ln10
	s_cmp_eq_u32 s46, 11
	s_cbranch_scc1 .Ln11
	s_cmp_eq_u32 s46, 12
	s_cbranch_scc1 .Ln12
	s_cmp_eq_u32 s46, 13
	s_cbranch_scc1 .Ln13
	s_cmp_eq_u32 s46, 14
	s_cbranch_scc1 .Ln14
	s_cmp_eq_u32 s46, 15
	s_cbranch_scc1 .Ln15
	s_cmp_eq_u32 s46, 16
	s_cbranch_scc1 .Ln16
